# baseline (speedup 1.0000x reference)
.LBB0_23:
	s_andn2_b64 vcc, exec, s[4:5]
	s_cbranch_vccnz .LBB0_43
	s_load_dwordx2 s[4:5], s[0:1], 0x0
	s_add_i32 s3, s2, 0xfffffdd6
	s_ashr_i32 s76, s3, 4
	s_sub_u32 s76, 0xff, s76
	v_lshlrev_b32_e32 v43, 3, v31
	v_lshl_or_b32 v2, s76, 5, v43
	v_lshrrev_b32_e32 v42, 8, v0
	s_lshl_b32 s3, s3, 1
	v_ashrrev_i32_e32 v3, 31, v2
	v_and_or_b32 v1, s3, 30, v42
	v_lshlrev_b64 v[2:3], 15, v[2:3]
	s_waitcnt lgkmcnt(0)
	v_lshl_add_u64 v[2:3], s[4:5], 0, v[2:3]
	v_lshlrev_b32_e32 v38, 10, v1
	v_mov_b32_e32 v39, 0
	v_lshl_add_u64 v[2:3], v[2:3], 0, v[38:39]
	v_lshlrev_b32_e32 v38, 4, v30
	v_lshl_add_u64 v[2:3], v[2:3], 0, v[38:39]
	s_mov_b32 s3, 0x8000
	v_add_co_u32_e32 v4, vcc, s3, v2
	s_mov_b32 s3, 0x10000
	s_nop 0
	v_addc_co_u32_e32 v5, vcc, 0, v3, vcc
	global_load_dwordx4 v[34:37], v[2:3], off nt
	global_load_dwordx4 v[26:29], v[4:5], off nt
	v_add_co_u32_e32 v4, vcc, s3, v2
	s_mov_b32 s3, 0x18000
	s_nop 0
	v_addc_co_u32_e32 v5, vcc, 0, v3, vcc
	v_add_co_u32_e32 v6, vcc, s3, v2
	s_mov_b32 s3, 0x20000
	s_nop 0
	v_addc_co_u32_e32 v7, vcc, 0, v3, vcc
	global_load_dwordx4 v[22:25], v[4:5], off nt
	global_load_dwordx4 v[18:21], v[6:7], off nt
	v_add_co_u32_e32 v4, vcc, s3, v2
	s_mov_b32 s3, 0x28000
	s_nop 0
	v_addc_co_u32_e32 v5, vcc, 0, v3, vcc
	v_add_co_u32_e32 v6, vcc, s3, v2
	s_mov_b32 s3, 0x30000
	s_nop 0
	v_addc_co_u32_e32 v7, vcc, 0, v3, vcc
	v_add_co_u32_e32 v32, vcc, s3, v2
	s_mov_b32 s3, 0x38000
	s_nop 0
	v_addc_co_u32_e32 v33, vcc, 0, v3, vcc
	v_add_co_u32_e32 v40, vcc, s3, v2
	global_load_dwordx4 v[14:17], v[4:5], off nt
	global_load_dwordx4 v[10:13], v[6:7], off nt
	v_addc_co_u32_e32 v41, vcc, 0, v3, vcc
	global_load_dwordx4 v[6:9], v[32:33], off nt
	global_load_dwordx4 v[2:5], v[40:41], off nt
	v_mbcnt_lo_u32_b32 v33, -1, 0
	v_mbcnt_hi_u32_b32 v33, -1, v33
	v_and_b32_e32 v40, 64, v33
	v_xor_b32_e32 v39, 1, v33
	v_add_u32_e32 v40, 64, v40
	v_cmp_lt_i32_e32 vcc, v39, v40
	v_mov_b32_e32 v32, 0x800
	v_lshl_or_b32 v32, v42, 10, v32
	v_cndmask_b32_e32 v33, v33, v39, vcc
	v_lshlrev_b32_e32 v33, 2, v33
	s_waitcnt vmcnt(7)
	v_cmp_neq_f32_e32 vcc, 0, v34
	s_nop 1
	v_cndmask_b32_e64 v34, 0, 1, vcc
	v_cmp_neq_f32_e32 vcc, 0, v35
	s_nop 1
	v_cndmask_b32_e64 v35, 0, 2, vcc
	v_cmp_neq_f32_e32 vcc, 0, v36
	v_or_b32_e32 v34, v35, v34
	s_nop 0
	v_cndmask_b32_e64 v36, 0, 4, vcc
	v_cmp_neq_f32_e32 vcc, 0, v37
	s_nop 1
	v_cndmask_b32_e64 v35, 0, 8, vcc
	v_or3_b32 v35, v34, v36, v35
	ds_bpermute_b32 v36, v33, v35
	v_and_b32_e32 v34, 1, v0
	v_cmp_eq_u32_e32 vcc, 0, v34
	v_or_b32_e32 v34, v32, v43
	v_add_u32_e32 v34, v34, v38
	s_and_saveexec_b64 s[4:5], vcc
	s_cbranch_execz .LBB0_26
	s_waitcnt lgkmcnt(0)
	v_lshl_or_b32 v35, v36, 4, v35
	ds_write_b8 v34, v35
